# MLA attention softmax: remaining half-swap copies removed (exp pairs keep registers of their own)
# speedup vs baseline: 1.0033x; 1.0023x over previous
.LBB0_829:
	v_mul_f32_e32 v151, 0x3e16c740, v2
	v_fma_f32 v36, v36, s3, -v151
	v_exp_f32_e32 v154, v36
	v_fma_f32 v36, v53, s3, -v151
	v_fma_f32 v52, v52, s3, -v151
	v_exp_f32_e32 v155, v36
	v_fma_f32 v36, v37, s3, -v151
	v_exp_f32_e32 v153, v52
	v_exp_f32_e32 v156, v36
	v_fma_f32 v36, v54, s3, -v151
	v_exp_f32_e32 v157, v36
	v_fma_f32 v36, v38, s3, -v151
	v_fma_f32 v38, v55, s3, -v151
	v_exp_f32_e32 v158, v36
	v_exp_f32_e32 v159, v38
	v_fma_f32 v38, v39, s3, -v151
	v_exp_f32_e32 v160, v38
	v_add_f32_e32 v52, v153, v154
	v_add_f32_e32 v36, 0, v52
	v_add_f32_e32 v37, v155, v156
	v_add_f32_e32 v36, v37, v36
	v_add_f32_e32 v37, v157, v158
	v_fma_f32 v38, v56, s3, -v151
	v_add_f32_e32 v36, v37, v36
	v_add_f32_e32 v37, v159, v160
	v_exp_f32_e32 v161, v38
	v_fma_f32 v38, v40, s3, -v151
	v_add_f32_e32 v40, v37, v36
	v_fma_f32 v36, v57, s3, -v151
	v_exp_f32_e32 v163, v36
	v_fma_f32 v36, v41, s3, -v151
	v_exp_f32_e32 v164, v36
	v_fma_f32 v36, v58, s3, -v151
	v_exp_f32_e32 v162, v38
	v_exp_f32_e32 v37, v36
	v_fma_f32 v36, v42, s3, -v151
	v_exp_f32_e32 v39, v36
	v_fma_f32 v36, v59, s3, -v151
	v_fma_f32 v38, v43, s3, -v151
	v_exp_f32_e32 v36, v36
	v_exp_f32_e32 v38, v38
	v_add_f32_e32 v52, v161, v162
	v_add_f32_e32 v40, v52, v40
	v_add_f32_e32 v41, v163, v164
	v_add_f32_e32 v42, v41, v40
	v_pk_add_f32 v[40:41], v[36:37], v[38:39]
	v_add_f32_e32 v41, v41, v42
	v_fma_f32 v42, v60, s3, -v151
	v_exp_f32_e32 v43, v42
	v_fma_f32 v42, v44, s3, -v151
	v_exp_f32_e32 v167, v42
	v_fma_f32 v42, v61, s3, -v151
	v_fma_f32 v44, v45, s3, -v151
	v_exp_f32_e32 v42, v42
	v_exp_f32_e32 v166, v44
	v_add_f32_e32 v44, v40, v41
	s_andn2_b64 vcc, exec, s[18:19]
	v_pk_add_f32 v[40:41], v[42:43], v[166:167]
	v_add_f32_e32 v41, v41, v44
	v_fma_f32 v44, v62, s3, -v151
	v_exp_f32_e32 v169, v44
	v_fma_f32 v44, v46, s3, -v151
	v_exp_f32_e32 v55, v44
	v_fma_f32 v44, v63, s3, -v151
	v_fma_f32 v46, v47, s3, -v151
	v_exp_f32_e32 v168, v44
	v_exp_f32_e32 v54, v46
	v_add_f32_e32 v46, v40, v41
	v_pk_add_f32 v[40:41], v[168:169], v[54:55]
	v_pk_mov_b32 v[54:55], v[54:55], v[54:55] op_sel:[1,0]
	v_add_f32_e32 v41, v41, v46
	v_fma_f32 v46, v64, s3, -v151
	v_exp_f32_e32 v47, v46
	v_fma_f32 v46, v48, s3, -v151
	v_exp_f32_e32 v171, v46
	v_fma_f32 v46, v65, s3, -v151
	v_fma_f32 v48, v49, s3, -v151
	v_exp_f32_e32 v46, v46
	v_exp_f32_e32 v170, v48
	v_add_f32_e32 v44, v40, v41
	v_fma_f32 v48, v51, s3, -v151
	v_exp_f32_e32 v172, v48
	v_pk_add_f32 v[40:41], v[46:47], v[170:171]
	v_add_f32_e32 v41, v41, v44
	v_fma_f32 v44, v66, s3, -v151
	v_exp_f32_e32 v175, v44
	v_fma_f32 v44, v50, s3, -v151
	v_exp_f32_e32 v173, v44
	v_fma_f32 v44, v67, s3, -v151
	v_exp_f32_e32 v174, v44
	v_add_f32_e32 v50, v40, v41
	v_pk_add_f32 v[40:41], v[174:175], v[172:173]
	v_add_f32_e32 v41, v41, v50
	v_add_f32_e32 v52, v40, v41
	ds_bpermute_b32 v53, v152, v52
	v_cvt_pk_bf16_f32 v48, v153, v155
	v_cvt_pk_bf16_f32 v49, v157, v159
	v_cvt_pk_bf16_f32 v50, v161, v163
	v_cvt_pk_bf16_f32 v51, v37, v36
	v_cvt_pk_bf16_f32 v44, v43, v42
	v_cvt_pk_bf16_f32 v45, v169, v168
	v_cvt_pk_bf16_f32 v46, v47, v46
	v_cvt_pk_bf16_f32 v47, v175, v174
	v_cvt_pk_bf16_f32 v40, v154, v156
	v_cvt_pk_bf16_f32 v41, v158, v160
	v_cvt_pk_bf16_f32 v42, v162, v164
	v_cvt_pk_bf16_f32 v43, v39, v38
	v_cvt_pk_bf16_f32 v36, v167, v166
	v_cvt_pk_bf16_f32 v37, v54, v55
	v_cvt_pk_bf16_f32 v38, v171, v170
	v_cvt_pk_bf16_f32 v39, v173, v172
	s_mov_b64 s[12:13], -1
	s_cbranch_vccnz .LBB0_832
	v_add3_u32 v58, s4, v146, v125
	v_add_u32_e32 v59, 0x3000, v58
	ds_read2_b64 v[54:57], v59 offset0:128 offset1:130
	v_add_u32_e32 v58, 0x4000, v58
	s_mov_b64 s[12:13], 0
	s_waitcnt lgkmcnt(0)
	v_mfma_f32_32x32x16_bf16 v[20:35], v[54:57], v[48:51], v[20:35]
	ds_read2_b64 v[54:57], v58 offset0:160 offset1:162
	s_waitcnt lgkmcnt(0)
	v_mfma_f32_32x32x16_bf16 v[4:19], v[54:57], v[48:51], v[4:19]
	ds_read2_b64 v[54:57], v59 offset0:132 offset1:134
	s_waitcnt lgkmcnt(0)
	v_mfma_f32_32x32x16_bf16 v[20:35], v[54:57], v[44:47], v[20:35]
	ds_read2_b64 v[54:57], v58 offset0:164 offset1:166
	s_waitcnt lgkmcnt(0)
	v_mfma_f32_32x32x16_bf16 v[4:19], v[54:57], v[44:47], v[4:19]
	ds_read2_b64 v[54:57], v59 offset0:136 offset1:138
	s_waitcnt lgkmcnt(0)
	v_mfma_f32_32x32x16_bf16 v[20:35], v[54:57], v[40:43], v[20:35]
	ds_read2_b64 v[54:57], v58 offset0:168 offset1:170
	s_waitcnt lgkmcnt(0)
	v_mfma_f32_32x32x16_bf16 v[4:19], v[54:57], v[40:43], v[4:19]
	ds_read2_b64 v[54:57], v59 offset0:140 offset1:142
	s_waitcnt lgkmcnt(0)
	v_mfma_f32_32x32x16_bf16 v[20:35], v[54:57], v[36:39], v[20:35]
	ds_read2_b64 v[54:57], v58 offset0:172 offset1:174
	s_waitcnt lgkmcnt(0)
	v_mfma_f32_32x32x16_bf16 v[4:19], v[54:57], v[36:39], v[4:19]
	s_branch .LBB0_833

.LBB0_845:
	v_mul_f32_e32 v2, 0x3e16c740, v69
	v_fma_f32 v36, v36, s3, -v2
	v_exp_f32_e32 v70, v36
	v_fma_f32 v36, v53, s3, -v2
	v_fma_f32 v52, v52, s3, -v2
	v_exp_f32_e32 v71, v36
	v_fma_f32 v36, v37, s3, -v2
	v_exp_f32_e32 v69, v52
	v_exp_f32_e32 v72, v36
	v_fma_f32 v36, v54, s3, -v2
	v_exp_f32_e32 v73, v36
	v_fma_f32 v36, v38, s3, -v2
	v_fma_f32 v38, v55, s3, -v2
	v_exp_f32_e32 v74, v36
	v_exp_f32_e32 v75, v38
	v_fma_f32 v38, v39, s3, -v2
	v_exp_f32_e32 v76, v38
	v_add_f32_e32 v52, v69, v70
	v_add_f32_e32 v36, 0, v52
	v_add_f32_e32 v37, v71, v72
	v_add_f32_e32 v36, v37, v36
	v_add_f32_e32 v37, v73, v74
	v_fma_f32 v38, v56, s3, -v2
	v_add_f32_e32 v36, v37, v36
	v_add_f32_e32 v37, v75, v76
	v_exp_f32_e32 v77, v38
	v_fma_f32 v38, v40, s3, -v2
	v_add_f32_e32 v40, v37, v36
	v_fma_f32 v36, v57, s3, -v2
	v_exp_f32_e32 v79, v36
	v_fma_f32 v36, v41, s3, -v2
	v_exp_f32_e32 v80, v36
	v_fma_f32 v36, v58, s3, -v2
	v_exp_f32_e32 v78, v38
	v_exp_f32_e32 v37, v36
	v_fma_f32 v36, v42, s3, -v2
	v_exp_f32_e32 v39, v36
	v_fma_f32 v36, v59, s3, -v2
	v_fma_f32 v38, v43, s3, -v2
	v_exp_f32_e32 v36, v36
	v_exp_f32_e32 v38, v38
	v_add_f32_e32 v52, v77, v78
	v_add_f32_e32 v40, v52, v40
	v_add_f32_e32 v41, v79, v80
	v_add_f32_e32 v42, v41, v40
	v_pk_add_f32 v[40:41], v[36:37], v[38:39]
	v_add_f32_e32 v41, v41, v42
	v_fma_f32 v42, v60, s3, -v2
	v_exp_f32_e32 v43, v42
	v_fma_f32 v42, v44, s3, -v2
	v_exp_f32_e32 v177, v42
	v_fma_f32 v42, v61, s3, -v2
	v_fma_f32 v44, v45, s3, -v2
	v_exp_f32_e32 v42, v42
	v_exp_f32_e32 v176, v44
	v_add_f32_e32 v44, v40, v41
	s_andn2_b64 vcc, exec, s[18:19]
	v_pk_add_f32 v[40:41], v[42:43], v[176:177]
	v_add_f32_e32 v41, v41, v44
	v_fma_f32 v44, v62, s3, -v2
	v_exp_f32_e32 v179, v44
	v_fma_f32 v44, v46, s3, -v2
	v_exp_f32_e32 v55, v44
	v_fma_f32 v44, v63, s3, -v2
	v_fma_f32 v46, v47, s3, -v2
	v_exp_f32_e32 v178, v44
	v_exp_f32_e32 v54, v46
	v_add_f32_e32 v46, v40, v41
	v_pk_add_f32 v[40:41], v[178:179], v[54:55]
	v_pk_mov_b32 v[54:55], v[54:55], v[54:55] op_sel:[1,0]
	v_add_f32_e32 v41, v41, v46
	v_fma_f32 v46, v64, s3, -v2
	v_exp_f32_e32 v47, v46
	v_fma_f32 v46, v48, s3, -v2
	v_exp_f32_e32 v181, v46
	v_fma_f32 v46, v65, s3, -v2
	v_fma_f32 v48, v49, s3, -v2
	v_exp_f32_e32 v46, v46
	v_exp_f32_e32 v180, v48
	v_add_f32_e32 v44, v40, v41
	s_mov_b64 s[4:5], -1
	v_pk_add_f32 v[40:41], v[46:47], v[180:181]
	s_nop 0
	v_add_f32_e32 v41, v41, v44
	v_fma_f32 v44, v66, s3, -v2
	v_exp_f32_e32 v183, v44
	v_fma_f32 v44, v50, s3, -v2
	v_exp_f32_e32 v185, v44
	v_fma_f32 v44, v67, s3, -v2
	v_fma_f32 v2, v51, s3, -v2
	v_exp_f32_e32 v182, v44
	v_exp_f32_e32 v184, v2
	v_add_f32_e32 v2, v40, v41
	v_pk_add_f32 v[40:41], v[182:183], v[184:185]
	v_add_f32_e32 v2, v41, v2
	v_add_f32_e32 v2, v40, v2
	ds_bpermute_b32 v52, v68, v2
	v_cvt_pk_bf16_f32 v48, v69, v71
	v_cvt_pk_bf16_f32 v49, v73, v75
	v_cvt_pk_bf16_f32 v50, v77, v79
	v_cvt_pk_bf16_f32 v51, v37, v36
	v_cvt_pk_bf16_f32 v44, v43, v42
	v_cvt_pk_bf16_f32 v45, v179, v178
	v_cvt_pk_bf16_f32 v46, v47, v46
	v_cvt_pk_bf16_f32 v47, v183, v182
	v_cvt_pk_bf16_f32 v40, v70, v72
	v_cvt_pk_bf16_f32 v41, v74, v76
	v_cvt_pk_bf16_f32 v42, v78, v80
	v_cvt_pk_bf16_f32 v43, v39, v38
	v_cvt_pk_bf16_f32 v36, v177, v176
	v_cvt_pk_bf16_f32 v37, v54, v55
	v_cvt_pk_bf16_f32 v38, v181, v180
	v_cvt_pk_bf16_f32 v39, v185, v184
	s_cbranch_vccnz .LBB0_847
	v_add3_u32 v53, s42, v146, v125
	v_add_u32_e32 v58, 0x3000, v53
	ds_read2_b64 v[54:57], v58 offset0:128 offset1:130
	v_add_u32_e32 v53, 0x4000, v53
	s_mov_b64 s[4:5], 0
	s_waitcnt lgkmcnt(0)
	v_mfma_f32_32x32x16_bf16 v[20:35], v[54:57], v[48:51], v[20:35]
	ds_read2_b64 v[54:57], v53 offset0:160 offset1:162
	s_waitcnt lgkmcnt(0)
	v_mfma_f32_32x32x16_bf16 v[4:19], v[54:57], v[48:51], v[4:19]
	ds_read2_b64 v[54:57], v58 offset0:132 offset1:134
	s_waitcnt lgkmcnt(0)
	v_mfma_f32_32x32x16_bf16 v[20:35], v[54:57], v[44:47], v[20:35]
	ds_read2_b64 v[54:57], v53 offset0:164 offset1:166
	s_waitcnt lgkmcnt(0)
	v_mfma_f32_32x32x16_bf16 v[4:19], v[54:57], v[44:47], v[4:19]
	ds_read2_b64 v[54:57], v58 offset0:136 offset1:138
	s_waitcnt lgkmcnt(0)
	v_mfma_f32_32x32x16_bf16 v[20:35], v[54:57], v[40:43], v[20:35]
	ds_read2_b64 v[54:57], v53 offset0:168 offset1:170
	s_waitcnt lgkmcnt(0)
	v_mfma_f32_32x32x16_bf16 v[4:19], v[54:57], v[40:43], v[4:19]
	ds_read2_b64 v[54:57], v58 offset0:140 offset1:142
	s_waitcnt lgkmcnt(0)
	v_mfma_f32_32x32x16_bf16 v[20:35], v[54:57], v[36:39], v[20:35]
	ds_read2_b64 v[54:57], v53 offset0:172 offset1:174
	s_waitcnt lgkmcnt(0)
	v_mfma_f32_32x32x16_bf16 v[4:19], v[54:57], v[36:39], v[4:19]
	s_branch .LBB0_848
